# first two counted waits of each in-proj / gate_up unit relaxed to vmcnt(8+NST) (NST = 16 / 8 epilogue stores of the previous unit stay in flight; strict vmcnt(8) for the first unit of a phase) on top
# baseline (speedup 1.0000x reference)
; #define PG8_LAS __attribute__((address_space(3)))
;     __device__ __forceinline__ void a_ready(const Unit&) const { if (++ncall == 3 && sig != nullptr && threadIdx.x == 0) __hip_atomic_fetch_add(sig, 1u, __ATOMIC_RELAXED, __HIP_MEMORY_SCOPE_AGENT); }
; #define PG8_STAGE(bufoff, gbase, voff) do { _Pragma("unroll") for (int _i = 0; _i < 2; ++_i) \
;         __builtin_amdgcn_global_load_lds((const unsigned*)((const char*)(gbase) + (voff)[_i]), (PG8_LAS unsigned*)(lds + (bufoff) + ldsw + _i * 8192), 16, 0, 0); } while (0)
; #define PG8_WAIT_V(n) asm volatile("s_waitcnt vmcnt(" #n ")" ::: "memory")
; #define PG8_BAR __builtin_amdgcn_s_barrier()
;     __device__ __forceinline__ void operator()(const f32x4 (&acc)[2][2][4][2], const Unit& u, int wr, int wc, int fr, int fq) const {
;         const int pn = u.pn, rl0 = wr * 64 + fr + (u.half == 2 ? HALF : 0), row0 = u.pm * BM + rl0, cl = wc * 32 + 8 * fq; const PG8_LAS float* rsr = rsl + rl0;
;         if (pn >= 4 && pn < 8) {
;             float qs_; asm volatile("s_mov_b32 %0, 0x3e38aa3b" : "=s"(qs_));
;             const bool isk = pn >= 6; bf16_t* dst = (bf16_t*)(wsb + (isk ? WS_K : WS_Q)); const float sc = isk ? 1.0f : qs_;
;             const int d0 = 16 * (wc & 1) + 4 * fq, hcol = ((pn & 1) * 4 + (wc >> 1)) * 64 + d0;
; template <class Epi, class Sched, bool ALIGN_EPI = false, bool SP2 = false>
; __device__ __forceinline__ void gemm_phase(PG8_LAS unsigned char* lds, const Gemm g, const Sched& S, const Epi& E) {
;     ...
;     const char* cA = (const char*)g.A + (size_t)cur.pm * tstep + (cur.half == 2 ? hstep : (size_t)0); const char* cB = (const char*)g.Bt + (size_t)cur.pn * tstep;
;     S.a_ready(cur);
;     if constexpr (SP2) {
;         PG8_STAGE(PG8_SB(0, 0), cB, voffB); PG8_STAGE(PG8_SB(0, 1), cB + hstep, voffB); PG8_STAGE(PG8_SA(0, 0), cA, voffA); PG8_STAGE(PG8_SA(0, 1), cA + hstep, voffA);
;         if (wr == 1) PG8_BAR;
;         PG8_WAIT_V(2); PG8_BAR;
;         if constexpr (Epi::ROWSCALE) stage_row_factors(rowp_, (PG8_LAS float*)E.rsl, tid);
;         PG8_STAGE(PG8_SB(1, 0), cB + kstep, voffB); PG8_STAGE(PG8_SA(1, 0), cA + kstep, voffA); PG8_STAGE(PG8_SB(1, 1), cB + hstep + kstep, voffB);
;         PG8_WAIT_V(6); PG8_BAR;
.LBB0_389:
	s_or_b64 exec, exec, s[6:7]
	s_add_u32 s35, s16, 0x500000
	s_addc_u32 s40, s17, 0
	s_and_b32 s12, s11, 3
	s_add_i32 m0, s19, 0x18000
	s_waitcnt vmcnt(0)
	v_lshl_add_u64 v[4:5], v[12:13], 0, s[42:43]
	s_lshl_b32 s6, s26, 13
	s_lshl_b32 s7, s12, 12
	global_load_lds_dwordx4 v[4:5], off
	v_lshl_add_u64 v[4:5], v[14:15], 0, s[42:43]
	s_add_i32 m0, s19, 0x1a000
	s_add_i32 s41, s19, 0x8000
	s_add_i32 s71, s19, 0xa000
	global_load_lds_dwordx4 v[4:5], off
	v_lshl_add_u64 v[4:5], v[10:11], 0, s[42:43]
	s_mov_b32 m0, s41
	s_add_u32 s4, s0, 0x40080
	global_load_lds_dwordx4 v[4:5], off
	v_lshl_add_u64 v[4:5], v[8:9], 0, s[42:43]
	s_mov_b32 m0, s71
	s_addc_u32 s5, s1, 0
	global_load_lds_dwordx4 v[4:5], off
	s_add_i32 m0, s19, 0x1c000
	v_lshl_add_u64 v[4:5], s[4:5], 0, v[166:167]
	global_load_lds_dwordx4 v[4:5], off
	v_lshl_add_u64 v[4:5], s[4:5], 0, v[170:171]
	s_add_i32 m0, s19, 0x1e000
	s_cmpk_lt_u32 s10, 0x100
	global_load_lds_dwordx4 v[4:5], off
	v_and_b32_e32 v4, 15, v2
	v_bfe_u32 v5, v2, 4, 2
	v_lshl_or_b32 v202, s26, 6, v4
	v_lshlrev_b32_e32 v7, 4, v5
	v_lshlrev_b32_e32 v8, 2, v202
	v_lshlrev_b32_e32 v2, 2, v2
	v_lshl_or_b32 v7, v4, 6, v7
	v_and_b32_e32 v9, 32, v8
	v_and_b32_e32 v2, 32, v2
	v_bitop3_b32 v9, v7, s6, v9 bitop3:0xde
	v_bitop3_b32 v203, v7, s7, v2 bitop3:0xde
	s_cselect_b64 s[58:59], -1, 0
	s_lshl_b32 s6, s11, 4
	v_lshlrev_b32_e32 v2, 2, v5
	v_and_or_b32 v204, s6, 16, v2
	s_lshl_b32 s10, s12, 1
	s_or_b32 s74, s10, -16
	s_add_i32 s10, 0, 0x20400
	v_lshlrev_b32_e32 v2, 2, v204
	v_lshlrev_b32_e32 v6, 3, v5
	v_cmp_eq_u32_e64 s[4:5], 0, v5
	s_bfe_u32 s73, s11, 0x10001
	v_cmp_eq_u32_e64 s[6:7], 0, v4
	v_add_u32_e32 v205, s10, v8
	v_lshl_add_u64 v[4:5], s[16:17], 0, v[2:3]
	s_mov_b64 s[10:11], 0x100000
	v_lshlrev_b32_e32 v2, 14, v16
	v_lshl_add_u64 v[174:175], v[4:5], 0, s[10:11]
	s_mov_b64 s[10:11], 0x300000
	v_and_b32_e32 v2, 0xffff8000, v2
	v_lshl_add_u64 v[176:177], v[4:5], 0, s[10:11]
	v_lshl_add_u32 v2, v17, 11, v2
	v_and_b32_e32 v4, 1, v16
	v_lshl_or_b32 v2, v4, 6, v2
	v_lshl_add_u32 v178, v18, 1, v2
	v_lshlrev_b32_e32 v2, 14, v19
	v_and_b32_e32 v2, 0xffff8000, v2
	s_waitcnt vmcnt(6)
	v_lshl_add_u32 v2, v20, 11, v2
	v_and_b32_e32 v4, 1, v19
	s_add_u32 s75, s16, 0xf000000
	v_lshl_or_b32 v2, v4, 6, v2
	v_lshl_or_b32 v172, s12, 5, v6
	v_mov_b32_e32 v173, v3
	s_mov_b32 s72, 0
	s_mov_b32 s32, 0
	s_addc_u32 s76, s17, 0
	v_mov_b32_e32 v179, v3
	v_lshl_add_u32 v180, v21, 1, v2
	v_mov_b32_e32 v181, v3
	v_add_u32_e32 v206, 0, v9
	s_barrier
	s_branch .LBB0_392

;     __device__ __forceinline__ void a_ready(const Unit&) const { if (++ncall == 3 && sig != nullptr && threadIdx.x == 0) __hip_atomic_fetch_add(sig, 1u, __ATOMIC_RELAXED, __HIP_MEMORY_SCOPE_AGENT); }
;     __device__ bool next(int i, Unit& u) const { if (!base.next(i >> 1, u)) return false; if (i & 1) { u.pm += MTOK / BM; u.pn += DM / BM; } return true; }
; #define PG8_STAGE(bufoff, gbase, voff) do { _Pragma("unroll") for (int _i = 0; _i < 2; ++_i) \
;         __builtin_amdgcn_global_load_lds((const unsigned*)((const char*)(gbase) + (voff)[_i]), (PG8_LAS unsigned*)(lds + (bufoff) + ldsw + _i * 8192), 16, 0, 0); } while (0)
; #define PG8_LDA(dst, b, h) do { _Pragma("unroll") for (int m = 0; m < 4; ++m) _Pragma("unroll") for (int k = 0; k < 2; ++k) dst[m][k] = *(const PG8_LAS bf16x8*)(lds + PG8_SA(b, h) + aoff + m * 2048 + k * 1024); } while (0)
; #define PG8_WAIT_V(n) asm volatile("s_waitcnt vmcnt(" #n ")" ::: "memory")
; #define PG8_WAIT_L(n) asm volatile("s_waitcnt lgkmcnt(" #n ")" ::: "memory")
; template <class Epi, class Sched, bool ALIGN_EPI = false, bool SP2 = false>
; __device__ __forceinline__ void gemm_phase(PG8_LAS unsigned char* lds, const Gemm g, const Sched& S, const Epi& E) {
;     ...
;         const bool has_next = S.next(ui + 1, nxt);
;         const char* nA = has_next ? (const char*)g.A + (size_t)nxt.pm * tstep + (nxt.half == 2 ? hstep : (size_t)0) : cA; const char* nB = has_next ? (const char*)g.Bt + (size_t)nxt.pn * tstep : cB;
;         for (int t = 0; t < nt; t += 2) {
;             const bool last = (t == nt - 2);
;             const char* a1 = cA + (size_t)(t + 1) * kstep;
;             const char* a2 = last ? nA : cA + (size_t)(t + 2) * kstep; const char* b2 = last ? nB : cB + (size_t)(t + 2) * kstep;
;             const char* a3 = a2 + kstep; const char* b3 = b2 + kstep;
;             if (last && has_next) S.a_ready(nxt);
;             if constexpr (SP2) {
;             PG8_LDB(B0, 0, 0); PG8_LDB(B1, 0, 1); PG8_SCHED; PG8_LDA(At, 0, 0); PG8_STAGE(PG8_SA(1, 1), a1 + hstep, voffA);
;     ...
;             if (PROBE_KIND == 18 && t == 0 && ui > 0 && g.probe) { const unsigned long long tq_ = __builtin_amdgcn_s_memrealtime(); PG8_WAIT_V(8); pg8_probe_acc += (unsigned)(__builtin_amdgcn_s_memrealtime() - tq_); }
;     ...
;             PG8_WAIT_V(8); PG8_WAIT_L(0); PG8_BAR; PG8_MMA(0, 0, At, B0); PG8_MMA(0, 1, At, B1); PG8_BAR; PG8_SCHED;
.LBB0_394:
	s_ashr_i32 s61, s60, 31
	s_lshl_b64 s[10:11], s[60:61], 19
	s_add_u32 s66, s24, s10
	s_addc_u32 s67, s25, s11
	s_and_b64 s[10:11], s[64:65], exec
	s_cselect_b32 s12, s67, s9
	s_cselect_b32 s13, s66, s8
	s_ashr_i32 s63, s62, 31
	s_lshl_b64 s[10:11], s[62:63], 19
	s_add_u32 s68, s28, s10
	s_addc_u32 s69, s29, s11
	s_and_b64 s[10:11], s[64:65], exec
	s_cselect_b32 s14, s69, s1
	s_cselect_b32 s15, s68, s0
	s_add_u32 s8, s8, 0x40080
	s_addc_u32 s9, s9, 0
	s_add_u32 s36, s0, 0x100
	s_addc_u32 s38, s1, 0
	s_mov_b32 s39, -2
	s_waitcnt lgkmcnt(0)
	s_add_u32 s0, s8, 0xfffc0080
	s_addc_u32 s1, s9, -1
	s_add_i32 s61, 0, 0x10000
	s_cmp_eq_u32 s39, 12
	s_cselect_b32 s11, s12, s1
	s_cselect_b32 s10, s13, s0
	v_add_u32_e32 v2, s61, v203
	s_cselect_b32 s1, s14, s38
	s_cselect_b32 s0, s15, s36
	s_add_i32 s63, 0, 0x14000
	ds_read_b128 v[132:135], v2
	ds_read_b128 v[136:139], v2 offset:1024
	ds_read_b128 v[140:143], v2 offset:2048
	ds_read_b128 v[144:147], v2 offset:3072
	v_add_u32_e32 v2, s63, v203
	ds_read_b128 v[148:151], v2
	ds_read_b128 v[152:155], v2 offset:1024
	ds_read_b128 v[156:159], v2 offset:2048
	ds_read_b128 v[160:163], v2 offset:3072
	v_lshl_add_u64 v[228:229], s[8:9], 0, v[178:179]
	s_add_i32 m0, s19, 0xc000
	ds_read_b128 v[182:185], v206
	ds_read_b128 v[186:189], v206 offset:1024
	ds_read_b128 v[190:193], v206 offset:2048
	ds_read_b128 v[194:197], v206 offset:3072
	ds_read_b128 v[198:201], v206 offset:4096
	ds_read_b128 v[208:211], v206 offset:5120
	ds_read_b128 v[212:215], v206 offset:6144
	ds_read_b128 v[216:219], v206 offset:7168
	global_load_lds_dwordx4 v[228:229], off
	v_lshl_add_u64 v[228:229], s[8:9], 0, v[180:181]
	s_add_i32 m0, s19, 0xe000
	s_nop 0
	global_load_lds_dwordx4 v[228:229], off
	s_cmp_eq_u32 s32, 0
	s_cbranch_scc1 .Lpw_ip_1
	s_waitcnt vmcnt(24)
	s_branch .Lpj_ip_1

; #define PG8_STAGE(bufoff, gbase, voff) do { _Pragma("unroll") for (int _i = 0; _i < 2; ++_i) \
;         __builtin_amdgcn_global_load_lds((const unsigned*)((const char*)(gbase) + (voff)[_i]), (PG8_LAS unsigned*)(lds + (bufoff) + ldsw + _i * 8192), 16, 0, 0); } while (0)
; #define PG8_LDA(dst, b, h) do { _Pragma("unroll") for (int m = 0; m < 4; ++m) _Pragma("unroll") for (int k = 0; k < 2; ++k) dst[m][k] = *(const PG8_LAS bf16x8*)(lds + PG8_SA(b, h) + aoff + m * 2048 + k * 1024); } while (0)
; #define PG8_MMA(ai, bj, At, Bt) do { __builtin_amdgcn_s_setprio(1); _Pragma("unroll") for (int m = 0; m < 4; ++m) _Pragma("unroll") for (int n = 0; n < 2; ++n) _Pragma("unroll") for (int k = 0; k < 2; ++k) \
;         acc[ai][bj][m][n] = __builtin_amdgcn_mfma_f32_16x16x32_bf16(Bt[n][k], At[m][k], acc[ai][bj][m][n], 0, 0, 0); __builtin_amdgcn_s_setprio(0); } while (0)
; #define PG8_WAIT_V(n) asm volatile("s_waitcnt vmcnt(" #n ")" ::: "memory")
; #define PG8_WAIT_L(n) asm volatile("s_waitcnt lgkmcnt(" #n ")" ::: "memory")
; #define PG8_BAR __builtin_amdgcn_s_barrier()
; #define PG8_SCHED __builtin_amdgcn_sched_barrier(0)
; template <class Epi, class Sched, bool ALIGN_EPI = false, bool SP2 = false>
; __device__ __forceinline__ void gemm_phase(PG8_LAS unsigned char* lds, const Gemm g, const Sched& S, const Epi& E) {
;     ...
;             PG8_WAIT_V(8); PG8_WAIT_L(0); PG8_BAR; PG8_MMA(0, 0, At, B0); PG8_MMA(0, 1, At, B1); PG8_BAR; PG8_SCHED;
;             PG8_LDA(At, 0, 1); PG8_STAGE(PG8_SB(0, 0), b2, voffB); PG8_STAGE(PG8_SB(0, 1), b2 + hstep, voffB); PG8_STAGE(PG8_SA(0, 0), a2, voffA);
;             PG8_WAIT_V(8); PG8_WAIT_L(0); PG8_BAR; if (cur.half == 0) { PG8_MMA(1, 0, At, B0); PG8_MMA(1, 1, At, B1); } PG8_BAR; PG8_SCHED;
.Lpj_ip_1:
	s_waitcnt lgkmcnt(0)
	s_barrier
	s_setprio 1
	s_waitcnt lgkmcnt(0)
	v_mfma_f32_16x16x32_bf16 v[128:131], v[132:135], v[182:185], 0
	v_mfma_f32_16x16x32_bf16 v[124:127], v[140:143], v[182:185], 0
	v_mfma_f32_16x16x32_bf16 v[112:115], v[132:135], v[190:193], 0
	v_mfma_f32_16x16x32_bf16 v[108:111], v[140:143], v[190:193], 0
	v_mfma_f32_16x16x32_bf16 v[96:99], v[132:135], v[198:201], 0
	v_mfma_f32_16x16x32_bf16 v[92:95], v[140:143], v[198:201], 0
	v_mfma_f32_16x16x32_bf16 v[80:83], v[132:135], v[212:215], 0
	v_mfma_f32_16x16x32_bf16 v[76:79], v[140:143], v[212:215], 0
	v_mfma_f32_16x16x32_bf16 v[128:131], v[136:139], v[186:189], v[128:131]
	v_mfma_f32_16x16x32_bf16 v[124:127], v[144:147], v[186:189], v[124:127]
	v_mfma_f32_16x16x32_bf16 v[112:115], v[136:139], v[194:197], v[112:115]
	v_mfma_f32_16x16x32_bf16 v[108:111], v[144:147], v[194:197], v[108:111]
	v_mfma_f32_16x16x32_bf16 v[96:99], v[136:139], v[208:211], v[96:99]
	v_mfma_f32_16x16x32_bf16 v[92:95], v[144:147], v[208:211], v[92:95]
	v_mfma_f32_16x16x32_bf16 v[80:83], v[136:139], v[216:219], v[80:83]
	v_mfma_f32_16x16x32_bf16 v[76:79], v[144:147], v[216:219], v[76:79]
	s_setprio 0
	s_setprio 1
	v_mfma_f32_16x16x32_bf16 v[120:123], v[148:151], v[182:185], 0
	v_mfma_f32_16x16x32_bf16 v[116:119], v[156:159], v[182:185], 0
	v_mfma_f32_16x16x32_bf16 v[104:107], v[148:151], v[190:193], 0
	v_mfma_f32_16x16x32_bf16 v[100:103], v[156:159], v[190:193], 0
	v_mfma_f32_16x16x32_bf16 v[88:91], v[148:151], v[198:201], 0
	v_mfma_f32_16x16x32_bf16 v[84:87], v[156:159], v[198:201], 0
	v_mfma_f32_16x16x32_bf16 v[72:75], v[148:151], v[212:215], 0
	v_mfma_f32_16x16x32_bf16 v[68:71], v[156:159], v[212:215], 0
	v_mfma_f32_16x16x32_bf16 v[120:123], v[152:155], v[186:189], v[120:123]
	v_mfma_f32_16x16x32_bf16 v[116:119], v[160:163], v[186:189], v[116:119]
	v_mfma_f32_16x16x32_bf16 v[104:107], v[152:155], v[194:197], v[104:107]
	v_mfma_f32_16x16x32_bf16 v[100:103], v[160:163], v[194:197], v[100:103]
	v_mfma_f32_16x16x32_bf16 v[88:91], v[152:155], v[208:211], v[88:91]
	v_mfma_f32_16x16x32_bf16 v[84:87], v[160:163], v[208:211], v[84:87]
	v_mfma_f32_16x16x32_bf16 v[72:75], v[152:155], v[216:219], v[72:75]
	v_mfma_f32_16x16x32_bf16 v[68:71], v[160:163], v[216:219], v[68:71]
	s_setprio 0
	s_barrier
	s_add_i32 s61, s61, s27
	v_lshl_add_u64 v[228:229], s[0:1], 0, v[166:167]
	s_mov_b32 m0, s61
	ds_read_b128 v[182:185], v206 offset:16384
	ds_read_b128 v[186:189], v206 offset:17408
	ds_read_b128 v[190:193], v206 offset:18432
	ds_read_b128 v[194:197], v206 offset:19456
	ds_read_b128 v[198:201], v206 offset:20480
	ds_read_b128 v[208:211], v206 offset:21504
	ds_read_b128 v[212:215], v206 offset:22528
	ds_read_b128 v[216:219], v206 offset:23552
	global_load_lds_dwordx4 v[228:229], off
	s_add_i32 m0, s61, 0x2000
	s_add_u32 s78, s0, 0x40000
	v_lshl_add_u64 v[230:231], s[0:1], 0, v[170:171]
	s_addc_u32 s79, s1, 0
	s_add_i32 s61, s63, s27
	global_load_lds_dwordx4 v[230:231], off
	v_lshl_add_u64 v[232:233], s[78:79], 0, v[166:167]
	s_mov_b32 m0, s61
	v_lshl_add_u64 v[234:235], s[10:11], 0, v[168:169]
	global_load_lds_dwordx4 v[232:233], off
	v_lshl_add_u64 v[232:233], s[78:79], 0, v[170:171]
	s_add_i32 m0, s61, 0x2000
	s_nop 0
	global_load_lds_dwordx4 v[232:233], off
	v_lshl_add_u64 v[232:233], s[10:11], 0, v[164:165]
	s_mov_b32 m0, s19
	s_nop 0
	global_load_lds_dwordx4 v[232:233], off
	s_mov_b32 m0, s30
	s_nop 0
	global_load_lds_dwordx4 v[234:235], off
	s_cmp_eq_u32 s32, 0
	s_cbranch_scc1 .Lpw_ip_2
	s_waitcnt vmcnt(24)
	s_branch .Lpj_ip_2

; #define PG8_STAGE(bufoff, gbase, voff) do { _Pragma("unroll") for (int _i = 0; _i < 2; ++_i) \
;         __builtin_amdgcn_global_load_lds((const unsigned*)((const char*)(gbase) + (voff)[_i]), (PG8_LAS unsigned*)(lds + (bufoff) + ldsw + _i * 8192), 16, 0, 0); } while (0)
; #define PG8_LDA(dst, b, h) do { _Pragma("unroll") for (int m = 0; m < 4; ++m) _Pragma("unroll") for (int k = 0; k < 2; ++k) dst[m][k] = *(const PG8_LAS bf16x8*)(lds + PG8_SA(b, h) + aoff + m * 2048 + k * 1024); } while (0)
; #define PG8_LDB(dst, b, h) do { _Pragma("unroll") for (int n = 0; n < 2; ++n) _Pragma("unroll") for (int k = 0; k < 2; ++k) dst[n][k] = *(const PG8_LAS bf16x8*)(lds + PG8_SB(b, h) + boff + n * 2048 + k * 1024); } while (0)
; #define PG8_MMA(ai, bj, At, Bt) do { __builtin_amdgcn_s_setprio(1); _Pragma("unroll") for (int m = 0; m < 4; ++m) _Pragma("unroll") for (int n = 0; n < 2; ++n) _Pragma("unroll") for (int k = 0; k < 2; ++k) \
;         acc[ai][bj][m][n] = __builtin_amdgcn_mfma_f32_16x16x32_bf16(Bt[n][k], At[m][k], acc[ai][bj][m][n], 0, 0, 0); __builtin_amdgcn_s_setprio(0); } while (0)
; #define PG8_WAIT_V(n) asm volatile("s_waitcnt vmcnt(" #n ")" ::: "memory")
; #define PG8_WAIT_L(n) asm volatile("s_waitcnt lgkmcnt(" #n ")" ::: "memory")
; #define PG8_BAR __builtin_amdgcn_s_barrier()
; #define PG8_SCHED __builtin_amdgcn_sched_barrier(0)
; template <class Epi, class Sched, bool ALIGN_EPI = false, bool SP2 = false>
; __device__ __forceinline__ void gemm_phase(PG8_LAS unsigned char* lds, const Gemm g, const Sched& S, const Epi& E) {
;     ...
;             PG8_WAIT_V(8); PG8_WAIT_L(0); PG8_BAR; if (cur.half == 0) { PG8_MMA(1, 0, At, B0); PG8_MMA(1, 1, At, B1); } PG8_BAR; PG8_SCHED;
;             PG8_LDB(B0, 1, 0); PG8_LDB(B1, 1, 1); PG8_SCHED; PG8_LDA(At, 1, 0); PG8_STAGE(PG8_SA(0, 1), a2 + hstep, voffA);
;             PG8_WAIT_V(8); PG8_WAIT_L(0); PG8_BAR; PG8_MMA(0, 0, At, B0); PG8_MMA(0, 1, At, B1); PG8_BAR; PG8_SCHED;
.Lpj_ip_2:
	s_waitcnt lgkmcnt(0)
	s_barrier
	s_setprio 1
	s_waitcnt lgkmcnt(0)
	v_mfma_f32_16x16x32_bf16 v[64:67], v[132:135], v[182:185], 0
	v_mfma_f32_16x16x32_bf16 v[60:63], v[140:143], v[182:185], 0
	v_mfma_f32_16x16x32_bf16 v[48:51], v[132:135], v[190:193], 0
	v_mfma_f32_16x16x32_bf16 v[44:47], v[140:143], v[190:193], 0
	v_mfma_f32_16x16x32_bf16 v[32:35], v[132:135], v[198:201], 0
	v_mfma_f32_16x16x32_bf16 v[28:31], v[140:143], v[198:201], 0
	v_mfma_f32_16x16x32_bf16 v[16:19], v[132:135], v[212:215], 0
	v_mfma_f32_16x16x32_bf16 v[12:15], v[140:143], v[212:215], 0
	v_mfma_f32_16x16x32_bf16 v[64:67], v[136:139], v[186:189], v[64:67]
	v_mfma_f32_16x16x32_bf16 v[60:63], v[144:147], v[186:189], v[60:63]
	v_mfma_f32_16x16x32_bf16 v[48:51], v[136:139], v[194:197], v[48:51]
	v_mfma_f32_16x16x32_bf16 v[44:47], v[144:147], v[194:197], v[44:47]
	v_mfma_f32_16x16x32_bf16 v[32:35], v[136:139], v[208:211], v[32:35]
	v_mfma_f32_16x16x32_bf16 v[28:31], v[144:147], v[208:211], v[28:31]
	v_mfma_f32_16x16x32_bf16 v[16:19], v[136:139], v[216:219], v[16:19]
	v_mfma_f32_16x16x32_bf16 v[12:15], v[144:147], v[216:219], v[12:15]
	s_setprio 0
	s_setprio 1
	v_mfma_f32_16x16x32_bf16 v[56:59], v[148:151], v[182:185], 0
	v_mfma_f32_16x16x32_bf16 v[52:55], v[156:159], v[182:185], 0
	v_mfma_f32_16x16x32_bf16 v[40:43], v[148:151], v[190:193], 0
	v_mfma_f32_16x16x32_bf16 v[36:39], v[156:159], v[190:193], 0
	v_mfma_f32_16x16x32_bf16 v[24:27], v[148:151], v[198:201], 0
	v_mfma_f32_16x16x32_bf16 v[20:23], v[156:159], v[198:201], 0
	v_mfma_f32_16x16x32_bf16 v[8:11], v[148:151], v[212:215], 0
	v_mfma_f32_16x16x32_bf16 v[4:7], v[156:159], v[212:215], 0
	v_mfma_f32_16x16x32_bf16 v[56:59], v[152:155], v[186:189], v[56:59]
	v_mfma_f32_16x16x32_bf16 v[52:55], v[160:163], v[186:189], v[52:55]
	v_mfma_f32_16x16x32_bf16 v[40:43], v[152:155], v[194:197], v[40:43]
	v_mfma_f32_16x16x32_bf16 v[36:39], v[160:163], v[194:197], v[36:39]
	v_mfma_f32_16x16x32_bf16 v[24:27], v[152:155], v[208:211], v[24:27]
	v_mfma_f32_16x16x32_bf16 v[20:23], v[160:163], v[208:211], v[20:23]
	v_mfma_f32_16x16x32_bf16 v[8:11], v[152:155], v[216:219], v[8:11]
	v_mfma_f32_16x16x32_bf16 v[4:7], v[160:163], v[216:219], v[4:7]
	s_setprio 0
	s_barrier
	s_add_i32 s61, 0, 0x18000
	v_add_u32_e32 v2, s61, v203
	s_add_i32 s63, 0, 0x1c000
	ds_read_b128 v[132:135], v2
	ds_read_b128 v[136:139], v2 offset:1024
	ds_read_b128 v[140:143], v2 offset:2048
	ds_read_b128 v[144:147], v2 offset:3072
	v_add_u32_e32 v2, s63, v203
	ds_read_b128 v[148:151], v2
	ds_read_b128 v[152:155], v2 offset:1024
	ds_read_b128 v[156:159], v2 offset:2048
	ds_read_b128 v[160:163], v2 offset:3072
	s_add_u32 s10, s10, 0x40000
	s_addc_u32 s11, s11, 0
	s_mov_b32 m0, s31
	v_lshl_add_u64 v[236:237], s[10:11], 0, v[164:165]
	ds_read_b128 v[182:185], v206 offset:32768
	ds_read_b128 v[186:189], v206 offset:33792
	ds_read_b128 v[190:193], v206 offset:34816
	ds_read_b128 v[194:197], v206 offset:35840
	ds_read_b128 v[198:201], v206 offset:36864
	ds_read_b128 v[208:211], v206 offset:37888
	ds_read_b128 v[212:215], v206 offset:38912
	ds_read_b128 v[216:219], v206 offset:39936
	global_load_lds_dwordx4 v[236:237], off
	v_lshl_add_u64 v[236:237], s[10:11], 0, v[168:169]
	s_mov_b32 m0, s34
	s_nop 0
	global_load_lds_dwordx4 v[236:237], off
	s_waitcnt vmcnt(8)
	s_waitcnt lgkmcnt(0)
	s_barrier
	s_setprio 1
	s_waitcnt lgkmcnt(0)
	v_mfma_f32_16x16x32_bf16 v[128:131], v[132:135], v[182:185], v[128:131]
	v_mfma_f32_16x16x32_bf16 v[124:127], v[140:143], v[182:185], v[124:127]
	v_mfma_f32_16x16x32_bf16 v[112:115], v[132:135], v[190:193], v[112:115]
	v_mfma_f32_16x16x32_bf16 v[108:111], v[140:143], v[190:193], v[108:111]
	v_mfma_f32_16x16x32_bf16 v[96:99], v[132:135], v[198:201], v[96:99]
	v_mfma_f32_16x16x32_bf16 v[92:95], v[140:143], v[198:201], v[92:95]
	v_mfma_f32_16x16x32_bf16 v[80:83], v[132:135], v[212:215], v[80:83]
	v_mfma_f32_16x16x32_bf16 v[76:79], v[140:143], v[212:215], v[76:79]
	v_mfma_f32_16x16x32_bf16 v[128:131], v[136:139], v[186:189], v[128:131]
	v_mfma_f32_16x16x32_bf16 v[124:127], v[144:147], v[186:189], v[124:127]
	v_mfma_f32_16x16x32_bf16 v[112:115], v[136:139], v[194:197], v[112:115]
	v_mfma_f32_16x16x32_bf16 v[108:111], v[144:147], v[194:197], v[108:111]
	v_mfma_f32_16x16x32_bf16 v[96:99], v[136:139], v[208:211], v[96:99]
	v_mfma_f32_16x16x32_bf16 v[92:95], v[144:147], v[208:211], v[92:95]
	v_mfma_f32_16x16x32_bf16 v[80:83], v[136:139], v[216:219], v[80:83]
	v_mfma_f32_16x16x32_bf16 v[76:79], v[144:147], v[216:219], v[76:79]
	s_setprio 0
	s_setprio 1
	v_mfma_f32_16x16x32_bf16 v[120:123], v[148:151], v[182:185], v[120:123]
	v_mfma_f32_16x16x32_bf16 v[116:119], v[156:159], v[182:185], v[116:119]
	v_mfma_f32_16x16x32_bf16 v[104:107], v[148:151], v[190:193], v[104:107]
	v_mfma_f32_16x16x32_bf16 v[100:103], v[156:159], v[190:193], v[100:103]
	v_mfma_f32_16x16x32_bf16 v[88:91], v[148:151], v[198:201], v[88:91]
	v_mfma_f32_16x16x32_bf16 v[84:87], v[156:159], v[198:201], v[84:87]
	v_mfma_f32_16x16x32_bf16 v[72:75], v[148:151], v[212:215], v[72:75]
	v_mfma_f32_16x16x32_bf16 v[68:71], v[156:159], v[212:215], v[68:71]
	v_mfma_f32_16x16x32_bf16 v[120:123], v[152:155], v[186:189], v[120:123]
	v_mfma_f32_16x16x32_bf16 v[116:119], v[160:163], v[186:189], v[116:119]
	v_mfma_f32_16x16x32_bf16 v[104:107], v[152:155], v[194:197], v[104:107]
	v_mfma_f32_16x16x32_bf16 v[100:103], v[160:163], v[194:197], v[100:103]
	v_mfma_f32_16x16x32_bf16 v[88:91], v[152:155], v[208:211], v[88:91]
	v_mfma_f32_16x16x32_bf16 v[84:87], v[160:163], v[208:211], v[84:87]
	v_mfma_f32_16x16x32_bf16 v[72:75], v[152:155], v[216:219], v[72:75]
	v_mfma_f32_16x16x32_bf16 v[68:71], v[160:163], v[216:219], v[68:71]
	s_setprio 0
	s_barrier
; #define PG8_STAGE(bufoff, gbase, voff) do { _Pragma("unroll") for (int _i = 0; _i < 2; ++_i) \
;         __builtin_amdgcn_global_load_lds((const unsigned*)((const char*)(gbase) + (voff)[_i]), (PG8_LAS unsigned*)(lds + (bufoff) + ldsw + _i * 8192), 16, 0, 0); } while (0)
; #define PG8_LDA(dst, b, h) do { _Pragma("unroll") for (int m = 0; m < 4; ++m) _Pragma("unroll") for (int k = 0; k < 2; ++k) dst[m][k] = *(const PG8_LAS bf16x8*)(lds + PG8_SA(b, h) + aoff + m * 2048 + k * 1024); } while (0)
; #define PG8_MMA(ai, bj, At, Bt) do { __builtin_amdgcn_s_setprio(1); _Pragma("unroll") for (int m = 0; m < 4; ++m) _Pragma("unroll") for (int n = 0; n < 2; ++n) _Pragma("unroll") for (int k = 0; k < 2; ++k) \
;         acc[ai][bj][m][n] = __builtin_amdgcn_mfma_f32_16x16x32_bf16(Bt[n][k], At[m][k], acc[ai][bj][m][n], 0, 0, 0); __builtin_amdgcn_s_setprio(0); } while (0)
; #define PG8_WAIT_V(n) asm volatile("s_waitcnt vmcnt(" #n ")" ::: "memory")
; #define PG8_WAIT_L(n) asm volatile("s_waitcnt lgkmcnt(" #n ")" ::: "memory")
; #define PG8_BAR __builtin_amdgcn_s_barrier()
; #define PG8_SCHED __builtin_amdgcn_sched_barrier(0)
; template <class Epi, class Sched, bool ALIGN_EPI = false, bool SP2 = false>
; __device__ __forceinline__ void gemm_phase(PG8_LAS unsigned char* lds, const Gemm g, const Sched& S, const Epi& E) {
;     ...
;             PG8_LDA(At, 1, 1); PG8_STAGE(PG8_SB(1, 0), b3, voffB); PG8_STAGE(PG8_SB(1, 1), b3 + hstep, voffB); PG8_STAGE(PG8_SA(1, 0), a3, voffA);
;             PG8_WAIT_V(8); PG8_WAIT_L(0); PG8_BAR; if (cur.half == 0) { PG8_MMA(1, 0, At, B0); PG8_MMA(1, 1, At, B1); } PG8_BAR; PG8_SCHED;
	s_add_i32 s10, s61, s27
	v_lshl_add_u64 v[228:229], v[228:229], 0, s[42:43]
	s_mov_b32 m0, s10
	ds_read_b128 v[182:185], v206 offset:49152
	ds_read_b128 v[186:189], v206 offset:50176
	ds_read_b128 v[190:193], v206 offset:51200
	ds_read_b128 v[194:197], v206 offset:52224
	ds_read_b128 v[198:201], v206 offset:53248
	ds_read_b128 v[208:211], v206 offset:54272
	ds_read_b128 v[212:215], v206 offset:55296
	ds_read_b128 v[216:219], v206 offset:56320
	global_load_lds_dwordx4 v[228:229], off
	s_add_i32 m0, s10, 0x2000
	s_add_u32 s0, s0, 0x40080
	v_lshl_add_u64 v[228:229], v[230:231], 0, s[42:43]
	s_addc_u32 s1, s1, 0
	s_add_i32 s10, s63, s27
	global_load_lds_dwordx4 v[228:229], off
	v_lshl_add_u64 v[228:229], s[0:1], 0, v[166:167]
	s_mov_b32 m0, s10
	s_nop 0
	global_load_lds_dwordx4 v[228:229], off
	v_lshl_add_u64 v[228:229], s[0:1], 0, v[170:171]
	s_add_i32 m0, s10, 0x2000
	s_nop 0
	global_load_lds_dwordx4 v[228:229], off
	v_lshl_add_u64 v[228:229], v[232:233], 0, s[42:43]
	s_mov_b32 m0, s41
	s_nop 0
	global_load_lds_dwordx4 v[228:229], off
	v_lshl_add_u64 v[228:229], v[234:235], 0, s[42:43]
	s_mov_b32 m0, s71
	s_nop 0
	global_load_lds_dwordx4 v[228:229], off
	s_waitcnt vmcnt(8)
	s_waitcnt lgkmcnt(0)
	s_barrier
	s_setprio 1
	s_waitcnt lgkmcnt(0)
	v_mfma_f32_16x16x32_bf16 v[64:67], v[132:135], v[182:185], v[64:67]
	v_mfma_f32_16x16x32_bf16 v[60:63], v[140:143], v[182:185], v[60:63]
	v_mfma_f32_16x16x32_bf16 v[48:51], v[132:135], v[190:193], v[48:51]
	v_mfma_f32_16x16x32_bf16 v[44:47], v[140:143], v[190:193], v[44:47]
	v_mfma_f32_16x16x32_bf16 v[32:35], v[132:135], v[198:201], v[32:35]
	v_mfma_f32_16x16x32_bf16 v[28:31], v[140:143], v[198:201], v[28:31]
	v_mfma_f32_16x16x32_bf16 v[16:19], v[132:135], v[212:215], v[16:19]
	v_mfma_f32_16x16x32_bf16 v[12:15], v[140:143], v[212:215], v[12:15]
	v_mfma_f32_16x16x32_bf16 v[64:67], v[136:139], v[186:189], v[64:67]
	v_mfma_f32_16x16x32_bf16 v[60:63], v[144:147], v[186:189], v[60:63]
	v_mfma_f32_16x16x32_bf16 v[48:51], v[136:139], v[194:197], v[48:51]
	v_mfma_f32_16x16x32_bf16 v[44:47], v[144:147], v[194:197], v[44:47]
	v_mfma_f32_16x16x32_bf16 v[32:35], v[136:139], v[208:211], v[32:35]
	v_mfma_f32_16x16x32_bf16 v[28:31], v[144:147], v[208:211], v[28:31]
	v_mfma_f32_16x16x32_bf16 v[16:19], v[136:139], v[216:219], v[16:19]
	v_mfma_f32_16x16x32_bf16 v[12:15], v[144:147], v[216:219], v[12:15]
	s_setprio 0
	s_setprio 1
	v_mfma_f32_16x16x32_bf16 v[56:59], v[148:151], v[182:185], v[56:59]
	v_mfma_f32_16x16x32_bf16 v[52:55], v[156:159], v[182:185], v[52:55]
	v_mfma_f32_16x16x32_bf16 v[40:43], v[148:151], v[190:193], v[40:43]
	v_mfma_f32_16x16x32_bf16 v[36:39], v[156:159], v[190:193], v[36:39]
	v_mfma_f32_16x16x32_bf16 v[24:27], v[148:151], v[198:201], v[24:27]
	v_mfma_f32_16x16x32_bf16 v[20:23], v[156:159], v[198:201], v[20:23]
	v_mfma_f32_16x16x32_bf16 v[8:11], v[148:151], v[212:215], v[8:11]
	v_mfma_f32_16x16x32_bf16 v[4:7], v[156:159], v[212:215], v[4:7]
	v_mfma_f32_16x16x32_bf16 v[56:59], v[152:155], v[186:189], v[56:59]
	v_mfma_f32_16x16x32_bf16 v[52:55], v[160:163], v[186:189], v[52:55]
	v_mfma_f32_16x16x32_bf16 v[40:43], v[152:155], v[194:197], v[40:43]
	v_mfma_f32_16x16x32_bf16 v[36:39], v[160:163], v[194:197], v[36:39]
	v_mfma_f32_16x16x32_bf16 v[24:27], v[152:155], v[208:211], v[24:27]
	v_mfma_f32_16x16x32_bf16 v[20:23], v[160:163], v[208:211], v[20:23]
	v_mfma_f32_16x16x32_bf16 v[8:11], v[152:155], v[216:219], v[8:11]
	v_mfma_f32_16x16x32_bf16 v[4:7], v[160:163], v[216:219], v[4:7]
	s_setprio 0
	s_barrier
	s_add_i32 s39, s39, 2
	s_add_u32 s8, s8, 0x100
	s_addc_u32 s9, s9, 0
	s_add_u32 s36, s36, 0x100
	s_addc_u32 s38, s38, 0
	s_mov_b32 s32, 1

; #define PG8_LAS __attribute__((address_space(3)))
;     __device__ __forceinline__ void a_ready(const Unit&) const { if (++ncall == 3 && sig != nullptr && threadIdx.x == 0) __hip_atomic_fetch_add(sig, 1u, __ATOMIC_RELAXED, __HIP_MEMORY_SCOPE_AGENT); }
; #define PG8_STAGE(bufoff, gbase, voff) do { _Pragma("unroll") for (int _i = 0; _i < 2; ++_i) \
;         __builtin_amdgcn_global_load_lds((const unsigned*)((const char*)(gbase) + (voff)[_i]), (PG8_LAS unsigned*)(lds + (bufoff) + ldsw + _i * 8192), 16, 0, 0); } while (0)
; #define PG8_WAIT_V(n) asm volatile("s_waitcnt vmcnt(" #n ")" ::: "memory")
; #define PG8_BAR __builtin_amdgcn_s_barrier()
; template <class Epi, class Sched, bool ALIGN_EPI = false, bool SP2 = false>
; __device__ __forceinline__ void gemm_phase(PG8_LAS unsigned char* lds, const Gemm g, const Sched& S, const Epi& E) {
;     ...
;     const char* cA = (const char*)g.A + (size_t)cur.pm * tstep + (cur.half == 2 ? hstep : (size_t)0); const char* cB = (const char*)g.Bt + (size_t)cur.pn * tstep;
;     S.a_ready(cur);
;     if constexpr (SP2) {
;         PG8_STAGE(PG8_SB(0, 0), cB, voffB); PG8_STAGE(PG8_SB(0, 1), cB + hstep, voffB); PG8_STAGE(PG8_SA(0, 0), cA, voffA); PG8_STAGE(PG8_SA(0, 1), cA + hstep, voffA);
;         if (wr == 1) PG8_BAR;
;         PG8_WAIT_V(2); PG8_BAR;
;         if constexpr (Epi::ROWSCALE) stage_row_factors(rowp_, (PG8_LAS float*)E.rsl, tid);
;         PG8_STAGE(PG8_SB(1, 0), cB + kstep, voffB); PG8_STAGE(PG8_SA(1, 0), cA + kstep, voffA); PG8_STAGE(PG8_SB(1, 1), cB + hstep + kstep, voffB);
;         PG8_WAIT_V(6); PG8_BAR;
.LBB0_1471:
	s_or_b64 exec, exec, s[16:17]
	s_or_b32 s16, s13, s19
	s_mov_b32 s13, s37
	s_lshl_b64 s[4:5], s[12:13], 20
	s_add_u32 s4, s10, s4
	s_addc_u32 s5, s11, s5
	s_mul_i32 s16, s16, 0x160000
	s_sub_u32 s4, s4, s16
	s_subb_u32 s5, s5, 0
	s_lshl_b32 s12, s29, 5
	s_and_b32 s17, s12, 0x60
	s_add_i32 m0, s15, 0x18000
	s_waitcnt vmcnt(0)
	v_lshl_add_u64 v[4:5], v[12:13], 0, s[42:43]
	s_lshl_b32 s16, s28, 13
	s_lshl_b32 s19, s17, 7
	global_load_lds_dwordx4 v[4:5], off
	v_lshl_add_u64 v[4:5], v[14:15], 0, s[42:43]
	s_add_i32 m0, s15, 0x1a000
	s_add_i32 s41, s15, 0x8000
	s_add_i32 s60, s15, 0xa000
	global_load_lds_dwordx4 v[4:5], off
	v_lshl_add_u64 v[4:5], v[10:11], 0, s[42:43]
	s_mov_b32 m0, s41
	s_add_u32 s12, s0, 0x40080
	global_load_lds_dwordx4 v[4:5], off
	v_lshl_add_u64 v[4:5], v[8:9], 0, s[42:43]
	s_mov_b32 m0, s60
	s_addc_u32 s13, s1, 0
	global_load_lds_dwordx4 v[4:5], off
	s_add_i32 m0, s15, 0x1c000
	v_lshl_add_u64 v[4:5], s[12:13], 0, v[2:3]
	global_load_lds_dwordx4 v[4:5], off
	v_lshl_add_u64 v[4:5], s[12:13], 0, v[136:137]
	s_add_i32 m0, s15, 0x1e000
	v_lshlrev_b32_e32 v8, 2, v16
	global_load_lds_dwordx4 v[4:5], off
	v_lshrrev_b32_e32 v5, 1, v16
	v_and_b32_e32 v4, 15, v16
	v_and_b32_e32 v5, 24, v5
	v_lshl_or_b32 v146, s28, 6, v4
	v_lshlrev_b32_e32 v6, 1, v5
	v_lshl_or_b32 v4, v4, 6, v6
	v_lshlrev_b32_e32 v6, 2, v146
	v_and_b32_e32 v7, 32, v6
	v_and_b32_e32 v8, 32, v8
	v_bitop3_b32 v7, v4, s16, v7 bitop3:0xde
	v_bitop3_b32 v147, v4, s19, v8 bitop3:0xde
	v_lshlrev_b32_e32 v4, 14, v17
	v_and_b32_e32 v4, 0xffff8000, v4
	v_or_b32_e32 v149, s17, v5
	v_lshl_add_u32 v4, v18, 11, v4
	v_and_b32_e32 v5, 1, v17
	v_lshl_or_b32 v4, v5, 6, v4
	v_lshl_add_u32 v138, v19, 1, v4
	v_lshlrev_b32_e32 v4, 14, v20
	v_and_b32_e32 v4, 0xffff8000, v4
	s_waitcnt vmcnt(6)
	s_cmpk_lt_u32 s18, 0x100
	v_lshl_add_u32 v4, v21, 11, v4
	v_and_b32_e32 v5, 1, v20
	s_cselect_b64 s[12:13], -1, 0
	s_add_i32 s16, 0, 0x20400
	v_lshl_or_b32 v4, v5, 6, v4
	v_add_u32_e32 v148, s16, v6
	v_mov_b32_e32 v139, v3
	v_lshl_add_u32 v140, v22, 1, v4
	v_mov_b32_e32 v141, v3
	s_mov_b32 s61, 0
	s_mov_b32 s32, 0
	v_add_u32_e32 v150, 0, v7
	s_barrier
	s_branch .LBB0_1474

;     __device__ __forceinline__ void a_ready(const Unit&) const { if (++ncall == 3 && sig != nullptr && threadIdx.x == 0) __hip_atomic_fetch_add(sig, 1u, __ATOMIC_RELAXED, __HIP_MEMORY_SCOPE_AGENT); }
;     __device__ bool next(int i, Unit& u) const { if (!base.next(i >> 1, u)) return false; if (i & 1) { u.pm += MTOK / BM; u.pn += DM / BM; } return true; }
; #define PG8_STAGE(bufoff, gbase, voff) do { _Pragma("unroll") for (int _i = 0; _i < 2; ++_i) \
;         __builtin_amdgcn_global_load_lds((const unsigned*)((const char*)(gbase) + (voff)[_i]), (PG8_LAS unsigned*)(lds + (bufoff) + ldsw + _i * 8192), 16, 0, 0); } while (0)
; #define PG8_LDA(dst, b, h) do { _Pragma("unroll") for (int m = 0; m < 4; ++m) _Pragma("unroll") for (int k = 0; k < 2; ++k) dst[m][k] = *(const PG8_LAS bf16x8*)(lds + PG8_SA(b, h) + aoff + m * 2048 + k * 1024); } while (0)
; #define PG8_WAIT_V(n) asm volatile("s_waitcnt vmcnt(" #n ")" ::: "memory")
; #define PG8_WAIT_L(n) asm volatile("s_waitcnt lgkmcnt(" #n ")" ::: "memory")
; template <class Epi, class Sched, bool ALIGN_EPI = false, bool SP2 = false>
; __device__ __forceinline__ void gemm_phase(PG8_LAS unsigned char* lds, const Gemm g, const Sched& S, const Epi& E) {
;     ...
;         const bool has_next = S.next(ui + 1, nxt);
;         const char* nA = has_next ? (const char*)g.A + (size_t)nxt.pm * tstep + (nxt.half == 2 ? hstep : (size_t)0) : cA; const char* nB = has_next ? (const char*)g.Bt + (size_t)nxt.pn * tstep : cB;
;         for (int t = 0; t < nt; t += 2) {
;             const bool last = (t == nt - 2);
;             const char* a1 = cA + (size_t)(t + 1) * kstep;
;             const char* a2 = last ? nA : cA + (size_t)(t + 2) * kstep; const char* b2 = last ? nB : cB + (size_t)(t + 2) * kstep;
;             const char* a3 = a2 + kstep; const char* b3 = b2 + kstep;
;             if (last && has_next) S.a_ready(nxt);
;             if constexpr (SP2) {
;             PG8_LDB(B0, 0, 0); PG8_LDB(B1, 0, 1); PG8_SCHED; PG8_LDA(At, 0, 0); PG8_STAGE(PG8_SA(1, 1), a1 + hstep, voffA);
;     ...
;             if (PROBE_KIND == 18 && t == 0 && ui > 0 && g.probe) { const unsigned long long tq_ = __builtin_amdgcn_s_memrealtime(); PG8_WAIT_V(8); pg8_probe_acc += (unsigned)(__builtin_amdgcn_s_memrealtime() - tq_); }
;     ...
;             PG8_WAIT_V(8); PG8_WAIT_L(0); PG8_BAR; PG8_MMA(0, 0, At, B0); PG8_MMA(0, 1, At, B1); PG8_BAR; PG8_SCHED;
.LBB0_1476:
	s_ashr_i32 s17, s16, 31
	s_lshl_b64 s[28:29], s[16:17], 19
	s_add_u32 s56, s30, s28
	s_addc_u32 s57, s31, s29
	s_and_b64 s[28:29], s[38:39], exec
	s_cselect_b32 s17, s57, s27
	s_cselect_b32 s62, s56, s26
	s_ashr_i32 s19, s18, 31
	s_lshl_b64 s[28:29], s[18:19], 19
	s_add_u32 s58, s34, s28
	s_addc_u32 s59, s35, s29
	s_and_b64 s[28:29], s[38:39], exec
	s_cselect_b32 s19, s59, s1
	s_cselect_b32 s63, s58, s0
	s_add_u32 s26, s26, 0x40080
	s_addc_u32 s27, s27, 0
	s_add_u32 s64, s0, 0x100
	s_addc_u32 s65, s1, 0
	s_mov_b32 s66, -2
	s_add_u32 s0, s26, 0xfffc0080
	s_addc_u32 s1, s27, -1
	s_add_i32 s67, 0, 0x10000
	s_cmp_eq_u32 s66, 12
	s_cselect_b32 s29, s17, s1
	s_cselect_b32 s28, s62, s0
	v_add_u32_e32 v151, s67, v147
	s_cselect_b32 s1, s19, s65
	s_cselect_b32 s0, s63, s64
	s_add_i32 s70, 0, 0x14000
	ds_read_b128 v[142:145], v151
	ds_read_b128 v[152:155], v151 offset:1024
	ds_read_b128 v[156:159], v151 offset:2048
	ds_read_b128 v[160:163], v151 offset:3072
	v_add_u32_e32 v151, s70, v147
	ds_read_b128 v[164:167], v151
	ds_read_b128 v[168:171], v151 offset:1024
	ds_read_b128 v[172:175], v151 offset:2048
	ds_read_b128 v[176:179], v151 offset:3072
	v_lshl_add_u64 v[212:213], s[26:27], 0, v[138:139]
	s_add_i32 m0, s15, 0xc000
	ds_read_b128 v[180:183], v150
	ds_read_b128 v[184:187], v150 offset:1024
	ds_read_b128 v[188:191], v150 offset:2048
	ds_read_b128 v[192:195], v150 offset:3072
	ds_read_b128 v[196:199], v150 offset:4096
	ds_read_b128 v[200:203], v150 offset:5120
	ds_read_b128 v[204:207], v150 offset:6144
	ds_read_b128 v[208:211], v150 offset:7168
	global_load_lds_dwordx4 v[212:213], off
	v_lshl_add_u64 v[212:213], s[26:27], 0, v[140:141]
	s_add_i32 m0, s15, 0xe000
	s_nop 0
	global_load_lds_dwordx4 v[212:213], off
	s_cmp_eq_u32 s32, 0
	s_cbranch_scc1 .Lpw_gu_1
	s_waitcnt vmcnt(16)
	s_branch .Lpj_gu_1

; #define PG8_STAGE(bufoff, gbase, voff) do { _Pragma("unroll") for (int _i = 0; _i < 2; ++_i) \
;         __builtin_amdgcn_global_load_lds((const unsigned*)((const char*)(gbase) + (voff)[_i]), (PG8_LAS unsigned*)(lds + (bufoff) + ldsw + _i * 8192), 16, 0, 0); } while (0)
; #define PG8_LDA(dst, b, h) do { _Pragma("unroll") for (int m = 0; m < 4; ++m) _Pragma("unroll") for (int k = 0; k < 2; ++k) dst[m][k] = *(const PG8_LAS bf16x8*)(lds + PG8_SA(b, h) + aoff + m * 2048 + k * 1024); } while (0)
; #define PG8_MMA(ai, bj, At, Bt) do { __builtin_amdgcn_s_setprio(1); _Pragma("unroll") for (int m = 0; m < 4; ++m) _Pragma("unroll") for (int n = 0; n < 2; ++n) _Pragma("unroll") for (int k = 0; k < 2; ++k) \
;         acc[ai][bj][m][n] = __builtin_amdgcn_mfma_f32_16x16x32_bf16(Bt[n][k], At[m][k], acc[ai][bj][m][n], 0, 0, 0); __builtin_amdgcn_s_setprio(0); } while (0)
; #define PG8_WAIT_V(n) asm volatile("s_waitcnt vmcnt(" #n ")" ::: "memory")
; #define PG8_WAIT_L(n) asm volatile("s_waitcnt lgkmcnt(" #n ")" ::: "memory")
; #define PG8_BAR __builtin_amdgcn_s_barrier()
; #define PG8_SCHED __builtin_amdgcn_sched_barrier(0)
; template <class Epi, class Sched, bool ALIGN_EPI = false, bool SP2 = false>
; __device__ __forceinline__ void gemm_phase(PG8_LAS unsigned char* lds, const Gemm g, const Sched& S, const Epi& E) {
;     ...
;             PG8_WAIT_V(8); PG8_WAIT_L(0); PG8_BAR; PG8_MMA(0, 0, At, B0); PG8_MMA(0, 1, At, B1); PG8_BAR; PG8_SCHED;
;             PG8_LDA(At, 0, 1); PG8_STAGE(PG8_SB(0, 0), b2, voffB); PG8_STAGE(PG8_SB(0, 1), b2 + hstep, voffB); PG8_STAGE(PG8_SA(0, 0), a2, voffA);
;             PG8_WAIT_V(8); PG8_WAIT_L(0); PG8_BAR; if (cur.half == 0) { PG8_MMA(1, 0, At, B0); PG8_MMA(1, 1, At, B1); } PG8_BAR; PG8_SCHED;
.Lpj_gu_1:
	s_waitcnt lgkmcnt(0)
	s_barrier
	s_setprio 1
	s_waitcnt lgkmcnt(0)
	v_mfma_f32_16x16x32_bf16 v[128:131], v[142:145], v[180:183], 0
	v_mfma_f32_16x16x32_bf16 v[124:127], v[156:159], v[180:183], 0
	v_mfma_f32_16x16x32_bf16 v[112:115], v[142:145], v[188:191], 0
	v_mfma_f32_16x16x32_bf16 v[108:111], v[156:159], v[188:191], 0
	v_mfma_f32_16x16x32_bf16 v[96:99], v[142:145], v[196:199], 0
	v_mfma_f32_16x16x32_bf16 v[92:95], v[156:159], v[196:199], 0
	v_mfma_f32_16x16x32_bf16 v[80:83], v[142:145], v[204:207], 0
	v_mfma_f32_16x16x32_bf16 v[76:79], v[156:159], v[204:207], 0
	v_mfma_f32_16x16x32_bf16 v[128:131], v[152:155], v[184:187], v[128:131]
	v_mfma_f32_16x16x32_bf16 v[124:127], v[160:163], v[184:187], v[124:127]
	v_mfma_f32_16x16x32_bf16 v[112:115], v[152:155], v[192:195], v[112:115]
	v_mfma_f32_16x16x32_bf16 v[108:111], v[160:163], v[192:195], v[108:111]
	v_mfma_f32_16x16x32_bf16 v[96:99], v[152:155], v[200:203], v[96:99]
	v_mfma_f32_16x16x32_bf16 v[92:95], v[160:163], v[200:203], v[92:95]
	v_mfma_f32_16x16x32_bf16 v[80:83], v[152:155], v[208:211], v[80:83]
	v_mfma_f32_16x16x32_bf16 v[76:79], v[160:163], v[208:211], v[76:79]
	s_setprio 0
	s_setprio 1
	v_mfma_f32_16x16x32_bf16 v[120:123], v[164:167], v[180:183], 0
	v_mfma_f32_16x16x32_bf16 v[116:119], v[172:175], v[180:183], 0
	v_mfma_f32_16x16x32_bf16 v[104:107], v[164:167], v[188:191], 0
	v_mfma_f32_16x16x32_bf16 v[100:103], v[172:175], v[188:191], 0
	v_mfma_f32_16x16x32_bf16 v[88:91], v[164:167], v[196:199], 0
	v_mfma_f32_16x16x32_bf16 v[84:87], v[172:175], v[196:199], 0
	v_mfma_f32_16x16x32_bf16 v[72:75], v[164:167], v[204:207], 0
	v_mfma_f32_16x16x32_bf16 v[68:71], v[172:175], v[204:207], 0
	v_mfma_f32_16x16x32_bf16 v[120:123], v[168:171], v[184:187], v[120:123]
	v_mfma_f32_16x16x32_bf16 v[116:119], v[176:179], v[184:187], v[116:119]
	v_mfma_f32_16x16x32_bf16 v[104:107], v[168:171], v[192:195], v[104:107]
	v_mfma_f32_16x16x32_bf16 v[100:103], v[176:179], v[192:195], v[100:103]
	v_mfma_f32_16x16x32_bf16 v[88:91], v[168:171], v[200:203], v[88:91]
	v_mfma_f32_16x16x32_bf16 v[84:87], v[176:179], v[200:203], v[84:87]
	v_mfma_f32_16x16x32_bf16 v[72:75], v[168:171], v[208:211], v[72:75]
	v_mfma_f32_16x16x32_bf16 v[68:71], v[176:179], v[208:211], v[68:71]
	s_setprio 0
	s_barrier
	s_add_i32 s67, s67, s25
	v_lshl_add_u64 v[212:213], s[0:1], 0, v[2:3]
	s_mov_b32 m0, s67
	ds_read_b128 v[180:183], v150 offset:16384
	ds_read_b128 v[184:187], v150 offset:17408
	ds_read_b128 v[188:191], v150 offset:18432
	ds_read_b128 v[192:195], v150 offset:19456
	ds_read_b128 v[196:199], v150 offset:20480
	ds_read_b128 v[200:203], v150 offset:21504
	ds_read_b128 v[204:207], v150 offset:22528
	ds_read_b128 v[208:211], v150 offset:23552
	global_load_lds_dwordx4 v[212:213], off
	s_add_i32 m0, s67, 0x2000
	s_add_u32 s68, s0, 0x40000
	v_lshl_add_u64 v[214:215], s[0:1], 0, v[136:137]
	s_addc_u32 s69, s1, 0
	s_add_i32 s67, s70, s25
	global_load_lds_dwordx4 v[214:215], off
	v_lshl_add_u64 v[216:217], s[68:69], 0, v[2:3]
	s_mov_b32 m0, s67
	v_lshl_add_u64 v[218:219], s[28:29], 0, v[134:135]
	global_load_lds_dwordx4 v[216:217], off
	v_lshl_add_u64 v[216:217], s[68:69], 0, v[136:137]
	s_add_i32 m0, s67, 0x2000
	s_nop 0
	global_load_lds_dwordx4 v[216:217], off
	v_lshl_add_u64 v[216:217], s[28:29], 0, v[132:133]
	s_mov_b32 m0, s15
	s_nop 0
	global_load_lds_dwordx4 v[216:217], off
	s_mov_b32 m0, s21
	s_nop 0
	global_load_lds_dwordx4 v[218:219], off
	s_cmp_eq_u32 s32, 0
	s_cbranch_scc1 .Lpw_gu_2
	s_waitcnt vmcnt(16)
	s_branch .Lpj_gu_2

; #define PG8_STAGE(bufoff, gbase, voff) do { _Pragma("unroll") for (int _i = 0; _i < 2; ++_i) \
;         __builtin_amdgcn_global_load_lds((const unsigned*)((const char*)(gbase) + (voff)[_i]), (PG8_LAS unsigned*)(lds + (bufoff) + ldsw + _i * 8192), 16, 0, 0); } while (0)
; #define PG8_LDA(dst, b, h) do { _Pragma("unroll") for (int m = 0; m < 4; ++m) _Pragma("unroll") for (int k = 0; k < 2; ++k) dst[m][k] = *(const PG8_LAS bf16x8*)(lds + PG8_SA(b, h) + aoff + m * 2048 + k * 1024); } while (0)
; #define PG8_LDB(dst, b, h) do { _Pragma("unroll") for (int n = 0; n < 2; ++n) _Pragma("unroll") for (int k = 0; k < 2; ++k) dst[n][k] = *(const PG8_LAS bf16x8*)(lds + PG8_SB(b, h) + boff + n * 2048 + k * 1024); } while (0)
; #define PG8_MMA(ai, bj, At, Bt) do { __builtin_amdgcn_s_setprio(1); _Pragma("unroll") for (int m = 0; m < 4; ++m) _Pragma("unroll") for (int n = 0; n < 2; ++n) _Pragma("unroll") for (int k = 0; k < 2; ++k) \
;         acc[ai][bj][m][n] = __builtin_amdgcn_mfma_f32_16x16x32_bf16(Bt[n][k], At[m][k], acc[ai][bj][m][n], 0, 0, 0); __builtin_amdgcn_s_setprio(0); } while (0)
; #define PG8_WAIT_V(n) asm volatile("s_waitcnt vmcnt(" #n ")" ::: "memory")
; #define PG8_WAIT_L(n) asm volatile("s_waitcnt lgkmcnt(" #n ")" ::: "memory")
; #define PG8_BAR __builtin_amdgcn_s_barrier()
; #define PG8_SCHED __builtin_amdgcn_sched_barrier(0)
; template <class Epi, class Sched, bool ALIGN_EPI = false, bool SP2 = false>
; __device__ __forceinline__ void gemm_phase(PG8_LAS unsigned char* lds, const Gemm g, const Sched& S, const Epi& E) {
;     ...
;             PG8_WAIT_V(8); PG8_WAIT_L(0); PG8_BAR; if (cur.half == 0) { PG8_MMA(1, 0, At, B0); PG8_MMA(1, 1, At, B1); } PG8_BAR; PG8_SCHED;
;             PG8_LDB(B0, 1, 0); PG8_LDB(B1, 1, 1); PG8_SCHED; PG8_LDA(At, 1, 0); PG8_STAGE(PG8_SA(0, 1), a2 + hstep, voffA);
;             PG8_WAIT_V(8); PG8_WAIT_L(0); PG8_BAR; PG8_MMA(0, 0, At, B0); PG8_MMA(0, 1, At, B1); PG8_BAR; PG8_SCHED;
.Lpj_gu_2:
	s_waitcnt lgkmcnt(0)
	s_barrier
	s_setprio 1
	s_waitcnt lgkmcnt(0)
	v_mfma_f32_16x16x32_bf16 v[64:67], v[142:145], v[180:183], 0
	v_mfma_f32_16x16x32_bf16 v[60:63], v[156:159], v[180:183], 0
	v_mfma_f32_16x16x32_bf16 v[48:51], v[142:145], v[188:191], 0
	v_mfma_f32_16x16x32_bf16 v[44:47], v[156:159], v[188:191], 0
	v_mfma_f32_16x16x32_bf16 v[32:35], v[142:145], v[196:199], 0
	v_mfma_f32_16x16x32_bf16 v[28:31], v[156:159], v[196:199], 0
	v_mfma_f32_16x16x32_bf16 v[16:19], v[142:145], v[204:207], 0
	v_mfma_f32_16x16x32_bf16 v[12:15], v[156:159], v[204:207], 0
	v_mfma_f32_16x16x32_bf16 v[64:67], v[152:155], v[184:187], v[64:67]
	v_mfma_f32_16x16x32_bf16 v[60:63], v[160:163], v[184:187], v[60:63]
	v_mfma_f32_16x16x32_bf16 v[48:51], v[152:155], v[192:195], v[48:51]
	v_mfma_f32_16x16x32_bf16 v[44:47], v[160:163], v[192:195], v[44:47]
	v_mfma_f32_16x16x32_bf16 v[32:35], v[152:155], v[200:203], v[32:35]
	v_mfma_f32_16x16x32_bf16 v[28:31], v[160:163], v[200:203], v[28:31]
	v_mfma_f32_16x16x32_bf16 v[16:19], v[152:155], v[208:211], v[16:19]
	v_mfma_f32_16x16x32_bf16 v[12:15], v[160:163], v[208:211], v[12:15]
	s_setprio 0
	s_setprio 1
	v_mfma_f32_16x16x32_bf16 v[56:59], v[164:167], v[180:183], 0
	v_mfma_f32_16x16x32_bf16 v[52:55], v[172:175], v[180:183], 0
	v_mfma_f32_16x16x32_bf16 v[40:43], v[164:167], v[188:191], 0
	v_mfma_f32_16x16x32_bf16 v[36:39], v[172:175], v[188:191], 0
	v_mfma_f32_16x16x32_bf16 v[24:27], v[164:167], v[196:199], 0
	v_mfma_f32_16x16x32_bf16 v[20:23], v[172:175], v[196:199], 0
	v_mfma_f32_16x16x32_bf16 v[8:11], v[164:167], v[204:207], 0
	v_mfma_f32_16x16x32_bf16 v[4:7], v[172:175], v[204:207], 0
	v_mfma_f32_16x16x32_bf16 v[56:59], v[168:171], v[184:187], v[56:59]
	v_mfma_f32_16x16x32_bf16 v[52:55], v[176:179], v[184:187], v[52:55]
	v_mfma_f32_16x16x32_bf16 v[40:43], v[168:171], v[192:195], v[40:43]
	v_mfma_f32_16x16x32_bf16 v[36:39], v[176:179], v[192:195], v[36:39]
	v_mfma_f32_16x16x32_bf16 v[24:27], v[168:171], v[200:203], v[24:27]
	v_mfma_f32_16x16x32_bf16 v[20:23], v[176:179], v[200:203], v[20:23]
	v_mfma_f32_16x16x32_bf16 v[8:11], v[168:171], v[208:211], v[8:11]
	v_mfma_f32_16x16x32_bf16 v[4:7], v[176:179], v[208:211], v[4:7]
	s_setprio 0
	s_barrier
	s_add_i32 s67, 0, 0x18000
	v_add_u32_e32 v151, s67, v147
	s_add_i32 s68, 0, 0x1c000
	ds_read_b128 v[142:145], v151
	ds_read_b128 v[152:155], v151 offset:1024
	ds_read_b128 v[156:159], v151 offset:2048
	ds_read_b128 v[160:163], v151 offset:3072
	v_add_u32_e32 v151, s68, v147
	ds_read_b128 v[164:167], v151
	ds_read_b128 v[168:171], v151 offset:1024
	ds_read_b128 v[172:175], v151 offset:2048
	ds_read_b128 v[176:179], v151 offset:3072
	s_add_u32 s28, s28, 0x40000
	s_addc_u32 s29, s29, 0
	s_mov_b32 m0, s36
	v_lshl_add_u64 v[220:221], s[28:29], 0, v[132:133]
	ds_read_b128 v[180:183], v150 offset:32768
	ds_read_b128 v[184:187], v150 offset:33792
	ds_read_b128 v[188:191], v150 offset:34816
	ds_read_b128 v[192:195], v150 offset:35840
	ds_read_b128 v[196:199], v150 offset:36864
	ds_read_b128 v[200:203], v150 offset:37888
	ds_read_b128 v[204:207], v150 offset:38912
	ds_read_b128 v[208:211], v150 offset:39936
	global_load_lds_dwordx4 v[220:221], off
	v_lshl_add_u64 v[220:221], s[28:29], 0, v[134:135]
	s_mov_b32 m0, s40
	s_nop 0
	global_load_lds_dwordx4 v[220:221], off
	s_waitcnt vmcnt(8)
	s_waitcnt lgkmcnt(0)
	s_barrier
	s_setprio 1
	s_waitcnt lgkmcnt(0)
	v_mfma_f32_16x16x32_bf16 v[128:131], v[142:145], v[180:183], v[128:131]
	v_mfma_f32_16x16x32_bf16 v[124:127], v[156:159], v[180:183], v[124:127]
	v_mfma_f32_16x16x32_bf16 v[112:115], v[142:145], v[188:191], v[112:115]
	v_mfma_f32_16x16x32_bf16 v[108:111], v[156:159], v[188:191], v[108:111]
	v_mfma_f32_16x16x32_bf16 v[96:99], v[142:145], v[196:199], v[96:99]
	v_mfma_f32_16x16x32_bf16 v[92:95], v[156:159], v[196:199], v[92:95]
	v_mfma_f32_16x16x32_bf16 v[80:83], v[142:145], v[204:207], v[80:83]
	v_mfma_f32_16x16x32_bf16 v[76:79], v[156:159], v[204:207], v[76:79]
	v_mfma_f32_16x16x32_bf16 v[128:131], v[152:155], v[184:187], v[128:131]
	v_mfma_f32_16x16x32_bf16 v[124:127], v[160:163], v[184:187], v[124:127]
	v_mfma_f32_16x16x32_bf16 v[112:115], v[152:155], v[192:195], v[112:115]
	v_mfma_f32_16x16x32_bf16 v[108:111], v[160:163], v[192:195], v[108:111]
	v_mfma_f32_16x16x32_bf16 v[96:99], v[152:155], v[200:203], v[96:99]
	v_mfma_f32_16x16x32_bf16 v[92:95], v[160:163], v[200:203], v[92:95]
	v_mfma_f32_16x16x32_bf16 v[80:83], v[152:155], v[208:211], v[80:83]
	v_mfma_f32_16x16x32_bf16 v[76:79], v[160:163], v[208:211], v[76:79]
	s_setprio 0
	s_setprio 1
	v_mfma_f32_16x16x32_bf16 v[120:123], v[164:167], v[180:183], v[120:123]
	v_mfma_f32_16x16x32_bf16 v[116:119], v[172:175], v[180:183], v[116:119]
	v_mfma_f32_16x16x32_bf16 v[104:107], v[164:167], v[188:191], v[104:107]
	v_mfma_f32_16x16x32_bf16 v[100:103], v[172:175], v[188:191], v[100:103]
	v_mfma_f32_16x16x32_bf16 v[88:91], v[164:167], v[196:199], v[88:91]
	v_mfma_f32_16x16x32_bf16 v[84:87], v[172:175], v[196:199], v[84:87]
	v_mfma_f32_16x16x32_bf16 v[72:75], v[164:167], v[204:207], v[72:75]
	v_mfma_f32_16x16x32_bf16 v[68:71], v[172:175], v[204:207], v[68:71]
	v_mfma_f32_16x16x32_bf16 v[120:123], v[168:171], v[184:187], v[120:123]
	v_mfma_f32_16x16x32_bf16 v[116:119], v[176:179], v[184:187], v[116:119]
	v_mfma_f32_16x16x32_bf16 v[104:107], v[168:171], v[192:195], v[104:107]
	v_mfma_f32_16x16x32_bf16 v[100:103], v[176:179], v[192:195], v[100:103]
	v_mfma_f32_16x16x32_bf16 v[88:91], v[168:171], v[200:203], v[88:91]
	v_mfma_f32_16x16x32_bf16 v[84:87], v[176:179], v[200:203], v[84:87]
	v_mfma_f32_16x16x32_bf16 v[72:75], v[168:171], v[208:211], v[72:75]
	v_mfma_f32_16x16x32_bf16 v[68:71], v[176:179], v[208:211], v[68:71]
	s_setprio 0
	s_barrier
; #define PG8_STAGE(bufoff, gbase, voff) do { _Pragma("unroll") for (int _i = 0; _i < 2; ++_i) \
;         __builtin_amdgcn_global_load_lds((const unsigned*)((const char*)(gbase) + (voff)[_i]), (PG8_LAS unsigned*)(lds + (bufoff) + ldsw + _i * 8192), 16, 0, 0); } while (0)
; #define PG8_LDA(dst, b, h) do { _Pragma("unroll") for (int m = 0; m < 4; ++m) _Pragma("unroll") for (int k = 0; k < 2; ++k) dst[m][k] = *(const PG8_LAS bf16x8*)(lds + PG8_SA(b, h) + aoff + m * 2048 + k * 1024); } while (0)
; #define PG8_MMA(ai, bj, At, Bt) do { __builtin_amdgcn_s_setprio(1); _Pragma("unroll") for (int m = 0; m < 4; ++m) _Pragma("unroll") for (int n = 0; n < 2; ++n) _Pragma("unroll") for (int k = 0; k < 2; ++k) \
;         acc[ai][bj][m][n] = __builtin_amdgcn_mfma_f32_16x16x32_bf16(Bt[n][k], At[m][k], acc[ai][bj][m][n], 0, 0, 0); __builtin_amdgcn_s_setprio(0); } while (0)
; #define PG8_WAIT_V(n) asm volatile("s_waitcnt vmcnt(" #n ")" ::: "memory")
; #define PG8_WAIT_L(n) asm volatile("s_waitcnt lgkmcnt(" #n ")" ::: "memory")
; #define PG8_BAR __builtin_amdgcn_s_barrier()
; #define PG8_SCHED __builtin_amdgcn_sched_barrier(0)
; template <class Epi, class Sched, bool ALIGN_EPI = false, bool SP2 = false>
; __device__ __forceinline__ void gemm_phase(PG8_LAS unsigned char* lds, const Gemm g, const Sched& S, const Epi& E) {
;     ...
;             PG8_LDA(At, 1, 1); PG8_STAGE(PG8_SB(1, 0), b3, voffB); PG8_STAGE(PG8_SB(1, 1), b3 + hstep, voffB); PG8_STAGE(PG8_SA(1, 0), a3, voffA);
;             PG8_WAIT_V(8); PG8_WAIT_L(0); PG8_BAR; if (cur.half == 0) { PG8_MMA(1, 0, At, B0); PG8_MMA(1, 1, At, B1); } PG8_BAR; PG8_SCHED;
	s_add_i32 s28, s67, s25
	v_lshl_add_u64 v[212:213], v[212:213], 0, s[42:43]
	s_mov_b32 m0, s28
	ds_read_b128 v[180:183], v150 offset:49152
	ds_read_b128 v[184:187], v150 offset:50176
	ds_read_b128 v[188:191], v150 offset:51200
	ds_read_b128 v[192:195], v150 offset:52224
	ds_read_b128 v[196:199], v150 offset:53248
	ds_read_b128 v[200:203], v150 offset:54272
	ds_read_b128 v[204:207], v150 offset:55296
	ds_read_b128 v[208:211], v150 offset:56320
	global_load_lds_dwordx4 v[212:213], off
	s_add_i32 m0, s28, 0x2000
	s_add_u32 s0, s0, 0x40080
	v_lshl_add_u64 v[212:213], v[214:215], 0, s[42:43]
	s_addc_u32 s1, s1, 0
	s_add_i32 s28, s68, s25
	global_load_lds_dwordx4 v[212:213], off
	v_lshl_add_u64 v[212:213], s[0:1], 0, v[2:3]
	s_mov_b32 m0, s28
	s_nop 0
	global_load_lds_dwordx4 v[212:213], off
	v_lshl_add_u64 v[212:213], s[0:1], 0, v[136:137]
	s_add_i32 m0, s28, 0x2000
	s_nop 0
	global_load_lds_dwordx4 v[212:213], off
	v_lshl_add_u64 v[212:213], v[216:217], 0, s[42:43]
	s_mov_b32 m0, s41
	s_nop 0
	global_load_lds_dwordx4 v[212:213], off
	v_lshl_add_u64 v[212:213], v[218:219], 0, s[42:43]
	s_mov_b32 m0, s60
	s_nop 0
	global_load_lds_dwordx4 v[212:213], off
	s_waitcnt vmcnt(8)
	s_waitcnt lgkmcnt(0)
	s_barrier
	s_setprio 1
	s_waitcnt lgkmcnt(0)
	v_mfma_f32_16x16x32_bf16 v[64:67], v[142:145], v[180:183], v[64:67]
	v_mfma_f32_16x16x32_bf16 v[60:63], v[156:159], v[180:183], v[60:63]
	v_mfma_f32_16x16x32_bf16 v[48:51], v[142:145], v[188:191], v[48:51]
	v_mfma_f32_16x16x32_bf16 v[44:47], v[156:159], v[188:191], v[44:47]
	v_mfma_f32_16x16x32_bf16 v[32:35], v[142:145], v[196:199], v[32:35]
	v_mfma_f32_16x16x32_bf16 v[28:31], v[156:159], v[196:199], v[28:31]
	v_mfma_f32_16x16x32_bf16 v[16:19], v[142:145], v[204:207], v[16:19]
	v_mfma_f32_16x16x32_bf16 v[12:15], v[156:159], v[204:207], v[12:15]
	v_mfma_f32_16x16x32_bf16 v[64:67], v[152:155], v[184:187], v[64:67]
	v_mfma_f32_16x16x32_bf16 v[60:63], v[160:163], v[184:187], v[60:63]
	v_mfma_f32_16x16x32_bf16 v[48:51], v[152:155], v[192:195], v[48:51]
	v_mfma_f32_16x16x32_bf16 v[44:47], v[160:163], v[192:195], v[44:47]
	v_mfma_f32_16x16x32_bf16 v[32:35], v[152:155], v[200:203], v[32:35]
	v_mfma_f32_16x16x32_bf16 v[28:31], v[160:163], v[200:203], v[28:31]
	v_mfma_f32_16x16x32_bf16 v[16:19], v[152:155], v[208:211], v[16:19]
	v_mfma_f32_16x16x32_bf16 v[12:15], v[160:163], v[208:211], v[12:15]
	s_setprio 0
	s_setprio 1
	v_mfma_f32_16x16x32_bf16 v[56:59], v[164:167], v[180:183], v[56:59]
	v_mfma_f32_16x16x32_bf16 v[52:55], v[172:175], v[180:183], v[52:55]
	v_mfma_f32_16x16x32_bf16 v[40:43], v[164:167], v[188:191], v[40:43]
	v_mfma_f32_16x16x32_bf16 v[36:39], v[172:175], v[188:191], v[36:39]
	v_mfma_f32_16x16x32_bf16 v[24:27], v[164:167], v[196:199], v[24:27]
	v_mfma_f32_16x16x32_bf16 v[20:23], v[172:175], v[196:199], v[20:23]
	v_mfma_f32_16x16x32_bf16 v[8:11], v[164:167], v[204:207], v[8:11]
	v_mfma_f32_16x16x32_bf16 v[4:7], v[172:175], v[204:207], v[4:7]
	v_mfma_f32_16x16x32_bf16 v[56:59], v[168:171], v[184:187], v[56:59]
	v_mfma_f32_16x16x32_bf16 v[52:55], v[176:179], v[184:187], v[52:55]
	v_mfma_f32_16x16x32_bf16 v[40:43], v[168:171], v[192:195], v[40:43]
	v_mfma_f32_16x16x32_bf16 v[36:39], v[176:179], v[192:195], v[36:39]
	v_mfma_f32_16x16x32_bf16 v[24:27], v[168:171], v[200:203], v[24:27]
	v_mfma_f32_16x16x32_bf16 v[20:23], v[176:179], v[200:203], v[20:23]
	v_mfma_f32_16x16x32_bf16 v[8:11], v[168:171], v[208:211], v[8:11]
	v_mfma_f32_16x16x32_bf16 v[4:7], v[176:179], v[208:211], v[4:7]
	s_setprio 0
	s_barrier
	s_add_i32 s66, s66, 2
	s_add_u32 s26, s26, 0x100
	s_addc_u32 s27, s27, 0
	s_add_u32 s64, s64, 0x100
	s_addc_u32 s65, s65, 0
	s_mov_b32 s32, 1
